# accumulator zeroing at GEMM unit start uses v_mov_b64 (64 instead of 128 moves) in all GEMM engines
# speedup vs baseline: 1.0246x; 1.0058x over previous
.LBB0_224:
	s_lshl_b32 s17, s45, 10
	s_and_b32 s17, s17, 0x400
	s_add_i32 s17, s17, 0
	s_lshl_b32 s15, s14, 8
	s_add_i32 s17, s17, 0x20000
	s_add_u32 s26, s26, 0x40080
	s_addc_u32 s27, s27, 0
	s_add_u32 s49, s28, 0x100
	v_mov_b32_e32 v4, 0
	s_addc_u32 s52, s29, 0
	s_mov_b32 s53, -2
	v_mov_b64_e32 v[4:5], 0
	v_mov_b64_e32 v[6:7], 0
	v_mov_b64_e32 v[8:9], 0
	v_mov_b64_e32 v[10:11], 0
	v_mov_b64_e32 v[12:13], 0
	v_mov_b64_e32 v[14:15], 0
	v_mov_b64_e32 v[16:17], 0
	v_mov_b64_e32 v[18:19], 0
	v_mov_b64_e32 v[20:21], 0
	v_mov_b64_e32 v[22:23], 0
	v_mov_b64_e32 v[24:25], 0
	v_mov_b64_e32 v[26:27], 0
	v_mov_b64_e32 v[28:29], 0
	v_mov_b64_e32 v[30:31], 0
	v_mov_b64_e32 v[32:33], 0
	v_mov_b64_e32 v[34:35], 0
	v_mov_b64_e32 v[36:37], 0
	v_mov_b64_e32 v[38:39], 0
	v_mov_b64_e32 v[40:41], 0
	v_mov_b64_e32 v[42:43], 0
	v_mov_b64_e32 v[44:45], 0
	v_mov_b64_e32 v[46:47], 0
	v_mov_b64_e32 v[48:49], 0
	v_mov_b64_e32 v[50:51], 0
	v_mov_b64_e32 v[52:53], 0
	v_mov_b64_e32 v[54:55], 0
	v_mov_b64_e32 v[56:57], 0
	v_mov_b64_e32 v[58:59], 0
	v_mov_b64_e32 v[60:61], 0
	v_mov_b64_e32 v[62:63], 0
	v_mov_b64_e32 v[64:65], 0
	v_mov_b64_e32 v[66:67], 0
	v_mov_b64_e32 v[68:69], 0
	v_mov_b64_e32 v[70:71], 0
	v_mov_b64_e32 v[72:73], 0
	v_mov_b64_e32 v[74:75], 0
	v_mov_b64_e32 v[76:77], 0
	v_mov_b64_e32 v[78:79], 0
	v_mov_b64_e32 v[80:81], 0
	v_mov_b64_e32 v[82:83], 0
	v_mov_b64_e32 v[84:85], 0
	v_mov_b64_e32 v[86:87], 0
	v_mov_b64_e32 v[88:89], 0
	v_mov_b64_e32 v[90:91], 0
	v_mov_b64_e32 v[92:93], 0
	v_mov_b64_e32 v[94:95], 0
	v_mov_b64_e32 v[96:97], 0
	v_mov_b64_e32 v[98:99], 0
	v_mov_b64_e32 v[100:101], 0
	v_mov_b64_e32 v[102:103], 0
	v_mov_b64_e32 v[104:105], 0
	v_mov_b64_e32 v[106:107], 0
	v_mov_b64_e32 v[108:109], 0
	v_mov_b64_e32 v[110:111], 0
	v_mov_b64_e32 v[112:113], 0
	v_mov_b64_e32 v[114:115], 0
	v_mov_b64_e32 v[116:117], 0
	v_mov_b64_e32 v[118:119], 0
	v_mov_b64_e32 v[120:121], 0
	v_mov_b64_e32 v[122:123], 0
	v_mov_b64_e32 v[124:125], 0
	v_mov_b64_e32 v[126:127], 0
	v_mov_b64_e32 v[128:129], 0
	v_mov_b64_e32 v[130:131], 0
	s_branch .LBB0_227

.LBB0_1975:
	s_lshl_b32 s38, s57, 10
	s_and_b32 s38, s38, 0x400
	s_add_i32 s59, s38, 0
	s_lshl_b32 s21, s20, 8
	s_add_i32 s59, s59, 0x20000
	s_add_u32 s34, s34, 0x40080
	s_addc_u32 s35, s35, 0
	s_add_u32 s62, s36, 0x100
	v_mov_b32_e32 v4, 0
	s_addc_u32 s63, s37, 0
	s_mov_b32 s64, -2
	v_mov_b64_e32 v[4:5], 0
	v_mov_b64_e32 v[6:7], 0
	v_mov_b64_e32 v[8:9], 0
	v_mov_b64_e32 v[10:11], 0
	v_mov_b64_e32 v[12:13], 0
	v_mov_b64_e32 v[14:15], 0
	v_mov_b64_e32 v[16:17], 0
	v_mov_b64_e32 v[18:19], 0
	v_mov_b64_e32 v[20:21], 0
	v_mov_b64_e32 v[22:23], 0
	v_mov_b64_e32 v[24:25], 0
	v_mov_b64_e32 v[26:27], 0
	v_mov_b64_e32 v[28:29], 0
	v_mov_b64_e32 v[30:31], 0
	v_mov_b64_e32 v[32:33], 0
	v_mov_b64_e32 v[34:35], 0
	v_mov_b64_e32 v[36:37], 0
	v_mov_b64_e32 v[38:39], 0
	v_mov_b64_e32 v[40:41], 0
	v_mov_b64_e32 v[42:43], 0
	v_mov_b64_e32 v[44:45], 0
	v_mov_b64_e32 v[46:47], 0
	v_mov_b64_e32 v[48:49], 0
	v_mov_b64_e32 v[50:51], 0
	v_mov_b64_e32 v[52:53], 0
	v_mov_b64_e32 v[54:55], 0
	v_mov_b64_e32 v[56:57], 0
	v_mov_b64_e32 v[58:59], 0
	v_mov_b64_e32 v[60:61], 0
	v_mov_b64_e32 v[62:63], 0
	v_mov_b64_e32 v[64:65], 0
	v_mov_b64_e32 v[66:67], 0
	v_mov_b64_e32 v[68:69], 0
	v_mov_b64_e32 v[70:71], 0
	v_mov_b64_e32 v[72:73], 0
	v_mov_b64_e32 v[74:75], 0
	v_mov_b64_e32 v[76:77], 0
	v_mov_b64_e32 v[78:79], 0
	v_mov_b64_e32 v[80:81], 0
	v_mov_b64_e32 v[82:83], 0
	v_mov_b64_e32 v[84:85], 0
	v_mov_b64_e32 v[86:87], 0
	v_mov_b64_e32 v[88:89], 0
	v_mov_b64_e32 v[90:91], 0
	v_mov_b64_e32 v[92:93], 0
	v_mov_b64_e32 v[94:95], 0
	v_mov_b64_e32 v[96:97], 0
	v_mov_b64_e32 v[98:99], 0
	v_mov_b64_e32 v[100:101], 0
	v_mov_b64_e32 v[102:103], 0
	v_mov_b64_e32 v[104:105], 0
	v_mov_b64_e32 v[106:107], 0
	v_mov_b64_e32 v[108:109], 0
	v_mov_b64_e32 v[110:111], 0
	v_mov_b64_e32 v[112:113], 0
	v_mov_b64_e32 v[114:115], 0
	v_mov_b64_e32 v[116:117], 0
	v_mov_b64_e32 v[118:119], 0
	v_mov_b64_e32 v[120:121], 0
	v_mov_b64_e32 v[122:123], 0
	v_mov_b64_e32 v[124:125], 0
	v_mov_b64_e32 v[126:127], 0
	v_mov_b64_e32 v[128:129], 0
	v_mov_b64_e32 v[130:131], 0
	s_branch .LBB0_1978

.LBB0_2055:
	s_cmp_lg_u32 s28, 3
	s_cselect_b64 s[30:31], -1, 0
	s_and_b64 s[30:31], s[30:31], exec
	s_cselect_b32 s31, s10, s48
	s_add_i32 s30, s28, 1
	s_cmp_lg_u32 s28, 3
	s_cselect_b64 s[62:63], -1, 0
	s_and_b64 s[28:29], s[62:63], exec
	s_cselect_b32 s28, s46, s47
	s_mul_i32 s50, s28, 0x2400
	s_cselect_b32 s58, s30, 0
	s_mul_hi_i32 s29, s28, 0x2400
	s_add_u32 s30, s20, s50
	s_mul_i32 s20, s58, 0x180
	s_addc_u32 s29, s21, s29
	s_ashr_i32 s21, s20, 31
	s_lshl_b64 s[20:21], s[20:21], 1
	s_add_u32 s20, s30, s20
	s_addc_u32 s21, s29, s21
	s_add_u32 s29, s20, 0x600
	s_addc_u32 s30, s21, 0
	s_ashr_i32 s59, s58, 31
	s_lshl_b64 s[20:21], s[58:59], 10
	s_ashr_i32 s50, s31, 31
	s_add_u32 s20, s20, s31
	s_addc_u32 s21, s21, s50
	s_mulk_i32 s21, 0x300
	s_mul_hi_u32 s31, s20, 0x300
	s_add_i32 s21, s31, s21
	s_mulk_i32 s20, 0x300
	s_add_u32 s31, s18, s20
	s_addc_u32 s58, s19, s21
	s_or_b64 s[18:19], s[62:63], s[14:15]
	s_cmp_gt_i32 s34, 1
	s_cselect_b32 s20, -2, 3
	s_add_i32 s59, s20, s34
	s_add_u32 s20, s26, 0xc0
	s_addc_u32 s21, s27, 0
	s_add_u32 s22, s22, 0xc0
	v_mov_b32_e32 v4, 0
	s_mov_b32 s28, 0
	s_addc_u32 s23, s23, 0
	s_movk_i32 s50, 0xfee0
	v_mov_b64_e32 v[4:5], 0
	v_mov_b64_e32 v[6:7], 0
	v_mov_b64_e32 v[8:9], 0
	v_mov_b64_e32 v[10:11], 0
	v_mov_b64_e32 v[12:13], 0
	v_mov_b64_e32 v[14:15], 0
	v_mov_b64_e32 v[16:17], 0
	v_mov_b64_e32 v[18:19], 0
	v_mov_b64_e32 v[20:21], 0
	v_mov_b64_e32 v[22:23], 0
	v_mov_b64_e32 v[24:25], 0
	v_mov_b64_e32 v[26:27], 0
	v_mov_b64_e32 v[28:29], 0
	v_mov_b64_e32 v[30:31], 0
	v_mov_b64_e32 v[32:33], 0
	v_mov_b64_e32 v[34:35], 0
	v_mov_b64_e32 v[36:37], 0
	v_mov_b64_e32 v[38:39], 0
	v_mov_b64_e32 v[40:41], 0
	v_mov_b64_e32 v[42:43], 0
	v_mov_b64_e32 v[44:45], 0
	v_mov_b64_e32 v[46:47], 0
	v_mov_b64_e32 v[48:49], 0
	v_mov_b64_e32 v[50:51], 0
	v_mov_b64_e32 v[52:53], 0
	v_mov_b64_e32 v[54:55], 0
	v_mov_b64_e32 v[56:57], 0
	v_mov_b64_e32 v[58:59], 0
	v_mov_b64_e32 v[60:61], 0
	v_mov_b64_e32 v[62:63], 0
	v_mov_b64_e32 v[64:65], 0
	v_mov_b64_e32 v[66:67], 0
	s_branch .LBB0_2057

.LBB0_2135:
	s_add_u32 s7, s18, 0x100
	s_waitcnt lgkmcnt(0)
	v_mov_b32_e32 v4, 0
	s_addc_u32 s44, s19, 0
	s_mov_b32 s45, -2
	v_mov_b64_e32 v[4:5], 0
	v_mov_b64_e32 v[6:7], 0
	v_mov_b64_e32 v[8:9], 0
	v_mov_b64_e32 v[10:11], 0
	v_mov_b64_e32 v[12:13], 0
	v_mov_b64_e32 v[14:15], 0
	v_mov_b64_e32 v[16:17], 0
	v_mov_b64_e32 v[18:19], 0
	v_mov_b64_e32 v[20:21], 0
	v_mov_b64_e32 v[22:23], 0
	v_mov_b64_e32 v[24:25], 0
	v_mov_b64_e32 v[26:27], 0
	v_mov_b64_e32 v[28:29], 0
	v_mov_b64_e32 v[30:31], 0
	v_mov_b64_e32 v[32:33], 0
	v_mov_b64_e32 v[34:35], 0
	v_mov_b64_e32 v[36:37], 0
	v_mov_b64_e32 v[38:39], 0
	v_mov_b64_e32 v[40:41], 0
	v_mov_b64_e32 v[42:43], 0
	v_mov_b64_e32 v[44:45], 0
	v_mov_b64_e32 v[46:47], 0
	v_mov_b64_e32 v[48:49], 0
	v_mov_b64_e32 v[50:51], 0
	v_mov_b64_e32 v[52:53], 0
	v_mov_b64_e32 v[54:55], 0
	v_mov_b64_e32 v[56:57], 0
	v_mov_b64_e32 v[58:59], 0
	v_mov_b64_e32 v[60:61], 0
	v_mov_b64_e32 v[62:63], 0
	v_mov_b64_e32 v[64:65], 0
	v_mov_b64_e32 v[66:67], 0
	v_mov_b64_e32 v[68:69], 0
	v_mov_b64_e32 v[70:71], 0
	v_mov_b64_e32 v[72:73], 0
	v_mov_b64_e32 v[74:75], 0
	v_mov_b64_e32 v[76:77], 0
	v_mov_b64_e32 v[78:79], 0
	v_mov_b64_e32 v[80:81], 0
	v_mov_b64_e32 v[82:83], 0
	v_mov_b64_e32 v[84:85], 0
	v_mov_b64_e32 v[86:87], 0
	v_mov_b64_e32 v[88:89], 0
	v_mov_b64_e32 v[90:91], 0
	v_mov_b64_e32 v[92:93], 0
	v_mov_b64_e32 v[94:95], 0
	v_mov_b64_e32 v[96:97], 0
	v_mov_b64_e32 v[98:99], 0
	v_mov_b64_e32 v[100:101], 0
	v_mov_b64_e32 v[102:103], 0
	v_mov_b64_e32 v[104:105], 0
	v_mov_b64_e32 v[106:107], 0
	v_mov_b64_e32 v[108:109], 0
	v_mov_b64_e32 v[110:111], 0
	v_mov_b64_e32 v[112:113], 0
	v_mov_b64_e32 v[114:115], 0
	v_mov_b64_e32 v[116:117], 0
	v_mov_b64_e32 v[118:119], 0
	v_mov_b64_e32 v[120:121], 0
	v_mov_b64_e32 v[122:123], 0
	v_mov_b64_e32 v[124:125], 0
	v_mov_b64_e32 v[126:127], 0
	v_mov_b64_e32 v[128:129], 0
	v_mov_b64_e32 v[130:131], 0

.LBB0_2370:
	s_lshl_b32 s2, s41, 19
	s_and_b32 s50, s2, 0x180000
	s_lshl_b32 s2, s42, 8
	s_and_b32 s44, s2, 0x100
	s_cmp_lt_i32 s41, 4
	v_ashrrev_i32_e32 v187, 31, v186
	s_cselect_b64 s[2:3], -1, 0
	s_lshl_b32 s4, s44, 2
	v_lshlrev_b64 v[6:7], 21, v[186:187]
	s_add_i32 s4, s4, 0
	v_lshl_add_u64 v[6:7], s[10:11], 0, v[6:7]
	s_add_i32 s4, s4, 0x20100
	v_lshl_add_u64 v[188:189], v[6:7], 0, s[50:51]
	v_ashrrev_i32_e32 v185, 31, v184
	v_lshl_add_u32 v240, v218, 2, s4
	v_lshl_add_u32 v241, v213, 2, s4
	s_mov_b64 s[4:5], 0x100
	v_cndmask_b32_e64 v239, v4, v188, s[0:1]
	v_lshlrev_b64 v[6:7], 19, v[184:185]
	v_mov_b32_e32 v193, v3
	v_mov_b32_e32 v197, v3
	v_lshl_add_u64 v[206:207], v[4:5], 0, s[4:5]
	v_mov_b32_e32 v4, 0
	v_cndmask_b32_e64 v191, v5, v189, s[0:1]
	v_lshl_add_u64 v[200:201], s[14:15], 0, v[6:7]
	v_lshl_add_u64 v[202:203], s[18:19], 0, v[196:197]
	v_lshl_add_u64 v[204:205], s[18:19], 0, v[192:193]
	s_mov_b32 s45, -2
	s_mov_b64 s[22:23], 0
	v_mov_b32_e32 v197, v196
	v_mov_b32_e32 v193, v198
	v_mov_b32_e32 v185, v194
	v_mov_b32_e32 v187, v192
	v_mov_b64_e32 v[4:5], 0
	v_mov_b64_e32 v[6:7], 0
	v_mov_b64_e32 v[8:9], 0
	v_mov_b64_e32 v[10:11], 0
	v_mov_b64_e32 v[12:13], 0
	v_mov_b64_e32 v[14:15], 0
	v_mov_b64_e32 v[16:17], 0
	v_mov_b64_e32 v[18:19], 0
	v_mov_b64_e32 v[20:21], 0
	v_mov_b64_e32 v[22:23], 0
	v_mov_b64_e32 v[24:25], 0
	v_mov_b64_e32 v[26:27], 0
	v_mov_b64_e32 v[28:29], 0
	v_mov_b64_e32 v[30:31], 0
	v_mov_b64_e32 v[32:33], 0
	v_mov_b64_e32 v[34:35], 0
	v_mov_b64_e32 v[36:37], 0
	v_mov_b64_e32 v[38:39], 0
	v_mov_b64_e32 v[40:41], 0
	v_mov_b64_e32 v[42:43], 0
	v_mov_b64_e32 v[44:45], 0
	v_mov_b64_e32 v[46:47], 0
	v_mov_b64_e32 v[48:49], 0
	v_mov_b64_e32 v[50:51], 0
	v_mov_b64_e32 v[52:53], 0
	v_mov_b64_e32 v[54:55], 0
	v_mov_b64_e32 v[56:57], 0
	v_mov_b64_e32 v[58:59], 0
	v_mov_b64_e32 v[60:61], 0
	v_mov_b64_e32 v[62:63], 0
	v_mov_b64_e32 v[64:65], 0
	v_mov_b64_e32 v[66:67], 0
	v_mov_b64_e32 v[68:69], 0
	v_mov_b64_e32 v[70:71], 0
	v_mov_b64_e32 v[72:73], 0
	v_mov_b64_e32 v[74:75], 0
	v_mov_b64_e32 v[76:77], 0
	v_mov_b64_e32 v[78:79], 0
	v_mov_b64_e32 v[80:81], 0
	v_mov_b64_e32 v[82:83], 0
	v_mov_b64_e32 v[84:85], 0
	v_mov_b64_e32 v[86:87], 0
	v_mov_b64_e32 v[88:89], 0
	v_mov_b64_e32 v[90:91], 0
	v_mov_b64_e32 v[92:93], 0
	v_mov_b64_e32 v[94:95], 0
	v_mov_b64_e32 v[96:97], 0
	v_mov_b64_e32 v[98:99], 0
	v_mov_b64_e32 v[100:101], 0
	v_mov_b64_e32 v[102:103], 0
	v_mov_b64_e32 v[104:105], 0
	v_mov_b64_e32 v[106:107], 0
	v_mov_b64_e32 v[108:109], 0
	v_mov_b64_e32 v[110:111], 0
	v_mov_b64_e32 v[112:113], 0
	v_mov_b64_e32 v[114:115], 0
	v_mov_b64_e32 v[116:117], 0
	v_mov_b64_e32 v[118:119], 0
	v_mov_b64_e32 v[120:121], 0
	v_mov_b64_e32 v[122:123], 0
	v_mov_b64_e32 v[124:125], 0
	v_mov_b64_e32 v[126:127], 0
	v_mov_b64_e32 v[128:129], 0
	v_mov_b64_e32 v[130:131], 0
	s_waitcnt vmcnt(0)
	s_branch .LBB0_2372

.LBB0_2450:
	s_add_u32 s22, s0, 0x80
	s_addc_u32 s23, s1, 0
	s_add_u32 s24, s4, 0x80
	v_mov_b32_e32 v4, 0
	s_addc_u32 s25, s5, 0
	s_mov_b32 s54, 0
	s_mov_b32 s55, 0
	v_mov_b64_e32 v[4:5], 0
	v_mov_b64_e32 v[6:7], 0
	v_mov_b64_e32 v[8:9], 0
	v_mov_b64_e32 v[10:11], 0
	v_mov_b64_e32 v[12:13], 0
	v_mov_b64_e32 v[14:15], 0
	v_mov_b64_e32 v[16:17], 0
	v_mov_b64_e32 v[18:19], 0
	v_mov_b64_e32 v[20:21], 0
	v_mov_b64_e32 v[22:23], 0
	v_mov_b64_e32 v[24:25], 0
	v_mov_b64_e32 v[26:27], 0
	v_mov_b64_e32 v[28:29], 0
	v_mov_b64_e32 v[30:31], 0
	v_mov_b64_e32 v[32:33], 0
	v_mov_b64_e32 v[34:35], 0
	v_mov_b64_e32 v[36:37], 0
	v_mov_b64_e32 v[38:39], 0
	v_mov_b64_e32 v[40:41], 0
	v_mov_b64_e32 v[42:43], 0
	v_mov_b64_e32 v[44:45], 0
	v_mov_b64_e32 v[46:47], 0
	v_mov_b64_e32 v[48:49], 0
	v_mov_b64_e32 v[50:51], 0
	v_mov_b64_e32 v[52:53], 0
	v_mov_b64_e32 v[54:55], 0
	v_mov_b64_e32 v[56:57], 0
	v_mov_b64_e32 v[58:59], 0
	v_mov_b64_e32 v[60:61], 0
	v_mov_b64_e32 v[62:63], 0
	v_mov_b64_e32 v[64:65], 0
	v_mov_b64_e32 v[66:67], 0
	v_mov_b64_e32 v[68:69], 0
	v_mov_b64_e32 v[70:71], 0
	v_mov_b64_e32 v[72:73], 0
	v_mov_b64_e32 v[74:75], 0
	v_mov_b64_e32 v[76:77], 0
	v_mov_b64_e32 v[78:79], 0
	v_mov_b64_e32 v[80:81], 0
	v_mov_b64_e32 v[82:83], 0
	v_mov_b64_e32 v[84:85], 0
	v_mov_b64_e32 v[86:87], 0
	v_mov_b64_e32 v[88:89], 0
	v_mov_b64_e32 v[90:91], 0
	v_mov_b64_e32 v[92:93], 0
	v_mov_b64_e32 v[94:95], 0
	v_mov_b64_e32 v[96:97], 0
	v_mov_b64_e32 v[98:99], 0
	v_mov_b64_e32 v[100:101], 0
	v_mov_b64_e32 v[102:103], 0
	v_mov_b64_e32 v[104:105], 0
	v_mov_b64_e32 v[106:107], 0
	v_mov_b64_e32 v[108:109], 0
	v_mov_b64_e32 v[110:111], 0
	v_mov_b64_e32 v[112:113], 0
	v_mov_b64_e32 v[114:115], 0
	v_mov_b64_e32 v[116:117], 0
	v_mov_b64_e32 v[118:119], 0
	v_mov_b64_e32 v[120:121], 0
	v_mov_b64_e32 v[122:123], 0
	v_mov_b64_e32 v[124:125], 0
	v_mov_b64_e32 v[126:127], 0
	v_mov_b64_e32 v[128:129], 0
	v_mov_b64_e32 v[130:131], 0
	s_branch .LBB0_2452

.LBB0_2570:
	s_ashr_i32 s22, s14, 7
	s_and_b32 s18, s15, 1
	v_lshlrev_b32_e32 v5, 2, v2
	s_lshl_b32 s23, s22, 12
	s_lshl_b32 s24, s18, 12
	v_and_b32_e32 v5, 48, v5
	v_lshlrev_b32_e32 v4, 6, v2
	v_sub_u32_e32 v5, 0, v5
	s_add_u32 s12, s12, 0xc0
	v_and_b32_e32 v4, 0x3c0, v4
	v_xor_b32_e32 v5, v2, v5
	s_addc_u32 s13, s13, 0
	v_and_or_b32 v71, v5, 48, v4
	s_add_u32 s14, s2, 0xc0
	v_mov_b32_e32 v4, 0
	s_mov_b32 s38, 0
	s_addc_u32 s15, s3, 0
	s_mov_b32 s39, 3
	s_mov_b32 s40, 0
	v_mov_b64_e32 v[4:5], 0
	v_mov_b64_e32 v[6:7], 0
	v_mov_b64_e32 v[8:9], 0
	v_mov_b64_e32 v[10:11], 0
	v_mov_b64_e32 v[12:13], 0
	v_mov_b64_e32 v[14:15], 0
	v_mov_b64_e32 v[16:17], 0
	v_mov_b64_e32 v[18:19], 0
	v_mov_b64_e32 v[20:21], 0
	v_mov_b64_e32 v[22:23], 0
	v_mov_b64_e32 v[24:25], 0
	v_mov_b64_e32 v[26:27], 0
	v_mov_b64_e32 v[28:29], 0
	v_mov_b64_e32 v[30:31], 0
	v_mov_b64_e32 v[32:33], 0
	v_mov_b64_e32 v[34:35], 0
	v_mov_b64_e32 v[36:37], 0
	v_mov_b64_e32 v[38:39], 0
	v_mov_b64_e32 v[40:41], 0
	v_mov_b64_e32 v[42:43], 0
	v_mov_b64_e32 v[44:45], 0
	v_mov_b64_e32 v[46:47], 0
	v_mov_b64_e32 v[48:49], 0
	v_mov_b64_e32 v[50:51], 0
	v_mov_b64_e32 v[52:53], 0
	v_mov_b64_e32 v[54:55], 0
	v_mov_b64_e32 v[56:57], 0
	v_mov_b64_e32 v[58:59], 0
	v_mov_b64_e32 v[60:61], 0
	v_mov_b64_e32 v[62:63], 0
	v_mov_b64_e32 v[64:65], 0
	v_mov_b64_e32 v[66:67], 0
	s_branch .LBB0_2572
